# v7 + P4 LoRA GEMM skips structurally-zero K-tiles (pn<8: K-tiles 0,1; pn>=8: K-tiles 2..5)
# speedup vs baseline: 1.0081x; 1.0081x over previous
;     __device__ bool next(int i, Unit& u) const { if (!StaticOrder::next(i >> 1, u)) return false; u.kh = i & 1; return true; }
;     __device__ bool next(int i, Unit& u) const { if (i >= 2) return false; u.pm = 0; u.pn = 0; u.e = 0; u.kh = 0; return true; }
;     __device__ bool next(int i, Unit& u) const { if (!StaticOrder::next(i, u)) return false; u.e = tile_e[u.pm]; return true; }
; #define PG8_STAGE(bufoff, gbase, voff) do { _Pragma("unroll") for (int _i = 0; _i < 2; ++_i) \
;         __builtin_amdgcn_global_load_lds((const unsigned*)((const char*)(gbase) + (voff)[_i]), (PG8_LAS unsigned*)(lds + (bufoff) + ldsw + _i * 8192), 16, 0, 0); } while (0)
; #define PG8_WAIT_V(n) asm volatile("s_waitcnt vmcnt(" #n ")" ::: "memory")
; #define PG8_BAR __builtin_amdgcn_s_barrier()
;     __host__ __device__ bool next(int i, Unit& u) const {
;         const long L = (long)i * G + c; if (L >= nwg) return false;
;         int wgid = (int)L; { const int q = nwg / NXCD, r = nwg % NXCD, xcd = wgid % NXCD, off = wgid / NXCD; wgid = (xcd < r ? xcd * (q + 1) : r * (q + 1) + (xcd - r) * q) + off; }
;         const int nig = WGM * nN, gid = wgid / nig, fm = gid * WGM, gsz = (nM - fm) < WGM ? (nM - fm) : WGM;
;         u.pm = fm + ((wgid % nig) % gsz); u.pn = (wgid % nig) / gsz; u.e = 0; u.kh = 0; return true;
; template <class Epi, class Sched, bool ALIGN_EPI = false, bool SP2 = false, bool GATHER = false, bool F8 = false>
; __device__ __forceinline__ void gemm_phase(PG8_LAS unsigned char* lds, const Gemm g, const Sched& S, const Epi& E) {
;     ...
;     const char* cA = (const char*)((Sched::PAIRS && cur.kh) ? g.A2 : g.A) + (GATHER ? (size_t)0 : (size_t)cur.pm * tstep); const char* cB = (const char*)((Sched::PAIRS && cur.kh) ? g.Bt2 : g.Bt) + (size_t)cur.e * g.bgs + (size_t)cur.pn * tstep;
;     S.a_ready(cur);
;     if constexpr (GATHER) load_gather(cur, gc0, gc1);
;     if constexpr (SP2) {
;         PG8_STAGE(PG8_SB(0, 0), cB, voffB); PG8_STAGE(PG8_SB(0, 1), cB + hstep, voffB); PG8_STAGE_A(PG8_SA(0, 0), cA, 0, false); PG8_STAGE_A(PG8_SA(0, 1), cA, 1, false);
;         if (wr == 1) PG8_BAR;
;         PG8_WAIT_V(2); PG8_BAR;
;         PG8_STAGE(PG8_SB(1, 0), cB + kstep, voffB); PG8_STAGE_A(PG8_SA(1, 0), cA + kstep, 0, false); PG8_STAGE(PG8_SB(1, 1), cB + hstep + kstep, voffB);
;         PG8_WAIT_V(6); PG8_BAR;
.LBB0_556:
	s_cmp_lt_i32 s24, 5
	s_cselect_b64 s[0:1], -1, 0
	s_cmp_gt_i32 s25, 4
	s_cselect_b64 s[2:3], -1, 0
	s_and_b64 s[0:1], s[0:1], s[2:3]
	s_andn2_b64 vcc, exec, s[0:1]
	s_cbranch_vccnz .LBB0_631
	v_readlane_b32 s0, v253, 2
	s_cmpk_gt_i32 s0, 0x2ff
	v_readfirstlane_b32 s0, v0
	s_cbranch_scc1 .LBB0_577
	s_waitcnt vmcnt(3)
	v_lshlrev_b32_e32 v1, 4, v0
	v_and_b32_e32 v2, 32, v0
	v_bitop3_b32 v1, v1, v2, 48 bitop3:0x6c
	v_bfe_u32 v3, v0, 2, 4
	s_waitcnt vmcnt(0)
	v_lshrrev_b32_e32 v10, 1, v1
	v_lshrrev_b32_e32 v1, 1, v0
	v_bfe_u32 v2, v0, 2, 2
	v_lshrrev_b32_e32 v4, 3, v0
	v_lshrrev_b32_e32 v6, 5, v0
	v_and_or_b32 v2, v1, 24, v2
	v_and_or_b32 v5, v4, 48, v3
	v_and_or_b32 v4, v4, 32, v6
	s_add_u32 s2, s50, 0x50000000
	v_and_b32_e32 v11, 32, v1
	v_and_or_b32 v4, v4, 36, v2
	s_addc_u32 s3, s51, 0
	v_mul_u32_u24_e32 v12, 0x180, v5
	v_or_b32_e32 v5, v11, v10
	v_mul_u32_u24_e32 v4, 0x180, v4
	s_add_u32 s20, s50, 0xe00000
	v_or_b32_e32 v4, v4, v5
	v_readlane_b32 s7, v253, 2
	s_addc_u32 s21, s51, 0
	v_lshlrev_b32_e32 v132, 1, v4
	v_bfe_u32 v4, v0, 3, 25
	s_ashr_i32 s23, s7, 31
	v_or_b32_e32 v4, 64, v4
	s_movk_i32 s1, 0x70
	s_lshr_b32 s4, s23, 29
	v_and_or_b32 v3, v4, s1, v3
	s_movk_i32 s1, 0x60
	s_add_i32 s4, s7, s4
	v_and_or_b32 v4, v4, s1, v6
	s_movk_i32 s1, 0x64
	s_lshr_b32 s5, s0, 6
	s_ashr_i32 s6, s4, 3
	s_and_b32 s4, s4, -8
	v_and_or_b32 v2, v4, s1, v2
	s_lshr_b32 s1, s0, 8
	s_lshl_b32 s22, s5, 10
	s_sub_i32 s4, s7, s4
	s_cmp_lt_i32 s4, 0
	s_movk_i32 s24, 0x61
	s_cselect_b32 s7, s24, 0x60
	s_mul_i32 s4, s4, s7
	s_add_i32 s4, s4, s6
	s_mul_hi_i32 s6, s4, 0x2aaaaaab
	s_lshr_b32 s7, s6, 31
	s_ashr_i32 s6, s6, 4
	s_add_i32 s6, s6, s7
	s_lshl_b32 s7, s6, 3
	s_mulk_i32 s6, 0x60
	s_sub_i32 s6, s4, s6
	s_bfe_i32 s4, s6, 0x80000
	s_bfe_u32 s4, s4, 0x3000c
	s_add_i32 s8, s6, s4
	s_bfe_i32 s4, s8, 0x80000
	s_and_b32 s8, s8, 0xf8
	s_sub_i32 s6, s6, s8
	s_sext_i32_i16 s9, s4
	s_sext_i32_i8 s6, s6
	s_add_i32 s61, s7, s6
	s_ashr_i32 s6, s9, 3
	s_cmp_ge_i32 s6, 8
	s_cselect_b32 s98, 0x100, 0
	s_cselect_b32 s99, 0, 2
	s_lshr_b32 s4, s9, 3
	s_mul_hi_i32 s7, s6, 0x30000
	s_mul_i32 s6, s6, 0x30000
	s_add_u32 s18, s20, s6
	s_addc_u32 s19, s21, s7
	s_add_u32 s18, s18, s98
	s_addc_u32 s19, s19, 0
	s_add_i32 s25, s22, 0
	v_mul_u32_u24_e32 v2, 0x180, v2
	s_add_i32 m0, s25, 0x10000
	v_or_b32_e32 v2, v2, v5
	global_load_lds_dwordx4 v132, s[18:19]
	s_add_i32 m0, s25, 0x12000
	v_lshlrev_b32_e32 v136, 1, v2
	s_add_u32 s6, s18, 0x18000
	global_load_lds_dwordx4 v136, s[18:19]
	s_addc_u32 s7, s19, 0
	s_add_i32 m0, s25, 0x14000
	s_mul_i32 s10, s61, 0x30000
	global_load_lds_dwordx4 v132, s[6:7]
	s_add_i32 m0, s25, 0x16000
	s_mul_hi_i32 s8, s61, 0x30000
	s_add_u32 s16, s2, s10
	v_or_b32_e32 v7, v12, v5
	v_mul_u32_u24_e32 v13, 0x180, v3
	s_addc_u32 s17, s3, s8
	s_add_u32 s16, s16, s98
	s_addc_u32 s17, s17, 0
	s_add_i32 s26, s25, 0x2000
	v_lshlrev_b32_e32 v130, 1, v7
	v_or_b32_e32 v3, v13, v5
	global_load_lds_dwordx4 v136, s[6:7]
	s_mov_b32 m0, s25
	s_add_u32 s6, s16, 0x18000
	v_lshlrev_b32_e32 v134, 1, v3
	global_load_lds_dwordx4 v130, s[16:17]
	s_mov_b32 m0, s26
	s_addc_u32 s7, s17, 0
	s_add_i32 s27, s25, 0x4000
	global_load_lds_dwordx4 v134, s[16:17]
	s_mov_b32 m0, s27
	s_add_i32 s28, s25, 0x6000
	global_load_lds_dwordx4 v130, s[6:7]
	s_mov_b32 m0, s28
	v_mov_b32_e32 v133, 0
	global_load_lds_dwordx4 v134, s[6:7]
	v_mov_b32_e32 v137, v133
	v_mov_b32_e32 v131, v133
	v_mov_b32_e32 v135, v133
	s_cmp_eq_u32 s1, 1
	s_mov_b32 s29, 0
	v_lshl_add_u64 v[8:9], s[18:19], 0, v[132:133]
	v_lshl_add_u64 v[6:7], s[18:19], 0, v[136:137]
	v_lshl_add_u64 v[2:3], s[16:17], 0, v[130:131]
	s_cselect_b64 s[6:7], -1, 0
	s_cmp_lg_u32 s1, 1
	v_lshl_add_u64 v[4:5], s[16:17], 0, v[134:135]
	s_cbranch_scc1 .LBB0_560
	s_barrier

; #define PG8_BAR __builtin_amdgcn_s_barrier()
; template <class Epi, class Sched, bool ALIGN_EPI = false, bool SP2 = false, bool GATHER = false, bool F8 = false>
; __device__ __forceinline__ void gemm_phase(PG8_LAS unsigned char* lds, const Gemm g, const Sched& S, const Epi& E) {
;     ...
;         if (!has_next) break;
;         if (!(Epi::MID && cur.kh == 0)) {
; #pragma unroll
;         for (int a = 0; a < 2; ++a)
; #pragma unroll
;             for (int b = 0; b < 2; ++b)
; #pragma unroll
;                 for (int m = 0; m < 4; ++m)
; #pragma unroll
;                     for (int n = 0; n < 2; ++n) acc[a][b][m][n] = (f32x4){0.f, 0.f, 0.f, 0.f}; }
;         cur = nxt; cA = nA; cB = nB; ++ui;
;         if constexpr (GATHER) { gc0[0] = gn0[0]; gc0[1] = gn0[1]; gc1[0] = gn1[0]; gc1[1] = gn1[1]; }
;         if constexpr (ALIGN_EPI) { if (wr == 1) PG8_BAR; }
.LBB0_562:
	s_andn2_b64 vcc, exec, s[4:5]
	s_mov_b32 s99, s98
	s_mov_b32 s62, s59
	s_mov_b32 s61, s60
	s_mov_b64 s[18:19], s[14:15]
	s_mov_b64 s[16:17], s[0:1]
	s_cbranch_vccz .LBB0_576

;     __device__ bool next(int i, Unit& u) const { if (!StaticOrder::next(i >> 1, u)) return false; u.kh = i & 1; return true; }
;     __device__ bool next(int i, Unit& u) const { if (i >= 2) return false; u.pm = 0; u.pn = 0; u.e = 0; u.kh = 0; return true; }
;     __device__ bool next(int i, Unit& u) const { if (!StaticOrder::next(i, u)) return false; u.e = tile_e[u.pm]; return true; }
; template <class Epi, class Sched, bool ALIGN_EPI = false, bool SP2 = false, bool GATHER = false, bool F8 = false>
; __device__ __forceinline__ void gemm_phase(PG8_LAS unsigned char* lds, const Gemm g, const Sched& S, const Epi& E) {
;     ...
;         const bool has_next = S.next(ui + 1, nxt);
;         const char* nA = has_next ? (const char*)((Sched::PAIRS && nxt.kh) ? g.A2 : g.A) + (GATHER ? (size_t)0 : (size_t)nxt.pm * tstep) : cA;
;         if constexpr (GATHER) { if (has_next) load_gather(nxt, gn0, gn1); else { gn0[0] = gc0[0]; gn0[1] = gc0[1]; gn1[0] = gc1[0]; gn1[1] = gc1[1]; } } const char* nB = has_next ? (const char*)((Sched::PAIRS && nxt.kh) ? g.Bt2 : g.Bt) + (size_t)nxt.e * g.bgs + (size_t)nxt.pn * tstep : cB;
;     ...
; #pragma unroll
;         for (int a = 0; a < 2; ++a)
; #pragma unroll
;             for (int b = 0; b < 2; ++b)
; #pragma unroll
;                 for (int m = 0; m < 4; ++m)
; #pragma unroll
;                     for (int n = 0; n < 2; ++n) acc[a][b][m][n] = (f32x4){0.f, 0.f, 0.f, 0.f}; }
.LBB0_565:
	s_nop 0
	v_cndmask_b32_e64 v2, 0, 1, s[0:1]
	v_cmp_ne_u32_e64 s[4:5], 1, v2
	s_andn2_b64 vcc, exec, s[0:1]
	s_mov_b64 s[0:1], s[16:17]
	s_cbranch_vccnz .LBB0_567
	s_mul_i32 s0, s60, 0x30000
	s_mul_hi_i32 s1, s60, 0x30000
	s_add_u32 s0, s2, s0
	s_addc_u32 s1, s3, s1
	s_cmp_ge_i32 s59, 8
	s_cselect_b32 s100, 0x100, 0
	s_add_u32 s0, s0, s100
	s_addc_u32 s1, s1, 0
.LBB0_567:
	s_and_b64 vcc, exec, s[4:5]
	s_mov_b64 s[14:15], s[18:19]
	s_cbranch_vccnz .LBB0_569
	s_mul_i32 s14, s59, 0x30000
	s_mul_hi_i32 s15, s59, 0x30000
	s_add_u32 s14, s20, s14
	s_addc_u32 s15, s21, s15
	s_cmp_ge_i32 s59, 8
	s_cselect_b32 s100, 0x100, 0
	s_cselect_b32 s98, 0, 2
	s_add_u32 s14, s14, s100
	s_addc_u32 s15, s15, 0
.LBB0_569:
	s_add_u32 s63, s18, 0x100
	v_mov_b32_e32 v2, 0
	s_addc_u32 s64, s19, 0
	s_mov_b32 s65, s99
	v_mov_b32_e32 v3, v2
	v_mov_b32_e32 v4, v2
	v_mov_b32_e32 v5, v2
	v_mov_b32_e32 v6, v2
	v_mov_b32_e32 v7, v2
	v_mov_b32_e32 v8, v2
	v_mov_b32_e32 v9, v2
	v_mov_b32_e32 v14, v2
	v_mov_b32_e32 v15, v2
	v_mov_b32_e32 v16, v2
	v_mov_b32_e32 v17, v2
	v_mov_b32_e32 v22, v2
	v_mov_b32_e32 v23, v2
	v_mov_b32_e32 v24, v2
	v_mov_b32_e32 v25, v2
	v_mov_b32_e32 v30, v2
	v_mov_b32_e32 v31, v2
	v_mov_b32_e32 v32, v2
	v_mov_b32_e32 v33, v2
	v_mov_b32_e32 v38, v2
	v_mov_b32_e32 v39, v2
	v_mov_b32_e32 v40, v2
	v_mov_b32_e32 v41, v2
	v_mov_b32_e32 v46, v2
	v_mov_b32_e32 v47, v2
	v_mov_b32_e32 v48, v2
	v_mov_b32_e32 v49, v2
	v_mov_b32_e32 v54, v2
	v_mov_b32_e32 v55, v2
	v_mov_b32_e32 v56, v2
	v_mov_b32_e32 v57, v2
	v_mov_b32_e32 v10, v2
	v_mov_b32_e32 v11, v2
	v_mov_b32_e32 v12, v2
	v_mov_b32_e32 v13, v2
	v_mov_b32_e32 v18, v2
	v_mov_b32_e32 v19, v2
	v_mov_b32_e32 v20, v2
	v_mov_b32_e32 v21, v2
	v_mov_b32_e32 v26, v2
	v_mov_b32_e32 v27, v2
	v_mov_b32_e32 v28, v2
	v_mov_b32_e32 v29, v2
	v_mov_b32_e32 v34, v2
	v_mov_b32_e32 v35, v2
	v_mov_b32_e32 v36, v2
	v_mov_b32_e32 v37, v2
	v_mov_b32_e32 v42, v2
	v_mov_b32_e32 v43, v2
	v_mov_b32_e32 v44, v2
	v_mov_b32_e32 v45, v2
	v_mov_b32_e32 v50, v2
	v_mov_b32_e32 v51, v2
	v_mov_b32_e32 v52, v2
	v_mov_b32_e32 v53, v2
	v_mov_b32_e32 v58, v2
	v_mov_b32_e32 v59, v2
	v_mov_b32_e32 v60, v2
	v_mov_b32_e32 v61, v2
	v_mov_b32_e32 v62, v2
	v_mov_b32_e32 v63, v2
	v_mov_b32_e32 v64, v2
	v_mov_b32_e32 v65, v2
	v_mov_b32_e32 v66, v2
	v_mov_b32_e32 v67, v2
	v_mov_b32_e32 v68, v2
	v_mov_b32_e32 v69, v2
	v_mov_b32_e32 v70, v2
	v_mov_b32_e32 v71, v2
	v_mov_b32_e32 v72, v2
	v_mov_b32_e32 v73, v2
	v_mov_b32_e32 v78, v2
	v_mov_b32_e32 v79, v2
	v_mov_b32_e32 v80, v2
	v_mov_b32_e32 v81, v2
	v_mov_b32_e32 v86, v2
	v_mov_b32_e32 v87, v2
	v_mov_b32_e32 v88, v2
	v_mov_b32_e32 v89, v2
	v_mov_b32_e32 v94, v2
	v_mov_b32_e32 v95, v2
	v_mov_b32_e32 v96, v2
	v_mov_b32_e32 v97, v2
	v_mov_b32_e32 v102, v2
	v_mov_b32_e32 v103, v2
	v_mov_b32_e32 v104, v2
	v_mov_b32_e32 v105, v2
	v_mov_b32_e32 v110, v2
	v_mov_b32_e32 v111, v2
	v_mov_b32_e32 v112, v2
	v_mov_b32_e32 v113, v2
	v_mov_b32_e32 v118, v2
	v_mov_b32_e32 v119, v2
	v_mov_b32_e32 v120, v2
	v_mov_b32_e32 v121, v2
	v_mov_b32_e32 v74, v2
	v_mov_b32_e32 v75, v2
	v_mov_b32_e32 v76, v2
	v_mov_b32_e32 v77, v2
	v_mov_b32_e32 v82, v2
	v_mov_b32_e32 v83, v2
	v_mov_b32_e32 v84, v2
	v_mov_b32_e32 v85, v2
	v_mov_b32_e32 v90, v2
	v_mov_b32_e32 v91, v2
	v_mov_b32_e32 v92, v2
	v_mov_b32_e32 v93, v2
	v_mov_b32_e32 v98, v2
	v_mov_b32_e32 v99, v2
	v_mov_b32_e32 v100, v2
	v_mov_b32_e32 v101, v2
	v_mov_b32_e32 v106, v2
	v_mov_b32_e32 v107, v2
	v_mov_b32_e32 v108, v2
	v_mov_b32_e32 v109, v2
	v_mov_b32_e32 v114, v2
	v_mov_b32_e32 v115, v2
	v_mov_b32_e32 v116, v2
	v_mov_b32_e32 v117, v2
	v_mov_b32_e32 v122, v2
	v_mov_b32_e32 v123, v2
	v_mov_b32_e32 v124, v2
	v_mov_b32_e32 v125, v2
	v_mov_b32_e32 v126, v2
	v_mov_b32_e32 v127, v2
	v_mov_b32_e32 v128, v2
	v_mov_b32_e32 v129, v2
